# attention-phase converter streams: loop-top wait covers the tile loads only, not the previous tile's two stores
# baseline (speedup 1.0000x reference)
; DEVI int opaque_tid() { int t = threadIdx.x; asm volatile("" : "+v"(t)); return t; }
; DEVI void cvt8_load(const Params& p, int L, int t, CvtIn& in) {
;     const int which = t / 4096, r = t % 4096, le = L * 16 + r / 256, kt = (r % 256) / 16, nt = r % 16;
;     const float* src = (which == 2 ? p.w_down : (which == 0 ? p.w_gate : p.w_up)) + (size_t)le * 2048 * 2048;
;     const int tid = opaque_tid(), nq = tid & 31, kq0 = tid >> 5;
; #pragma unroll
;     for (int it = 0; it < 2; ++it)
; #pragma unroll
;         for (int kk = 0; kk < 4; ++kk) in.v[it * 4 + kk] = __builtin_nontemporal_load((const f32x4*)(src + (size_t)(kt * 128 + (kq0 + it * 16) * 4 + kk) * 2048 + nt * 128 + nq * 4));
; }
; DEVI void cvt8_stream3(const Params& p, int L, int t0, int step, int count, char* smem) {
;     if (count <= 0) return;
;     CvtIn a, b; cvt8_load(p, L, t0, a);
;     if (count > 1) cvt8_load(p, L, t0 + step, b);
; #pragma nounroll
;     for (int i = 0; i < count; ++i) { CvtIn c;
;         if (i + 2 < count) cvt8_load(p, L, t0 + (i + 2) * step, c);
;         cvt8_finish(p, L, t0 + i * step, a, smem);
;         a = b; b = c; }
.LBB0_773:
	s_and_b64 vcc, exec, s[16:17]
	s_cbranch_vccz .LBB0_801
	v_readlane_b32 s4, v255, 0
	v_readlane_b32 s5, v255, 1
	s_mov_b32 s6, s2
	s_mov_b64 s[16:17], -1
	s_and_b64 vcc, exec, s[4:5]
	s_cbranch_vccz .LBB0_784
	s_add_i32 s7, s6, 0x1cd0
	s_and_b32 s4, s7, 0xfffff000
	s_add_i32 s5, s6, 0x2ccf
	s_cmpk_lt_u32 s5, 0x1fff
	s_cselect_b32 s5, s64, 0x80
	s_cmpk_lg_i32 s4, 0x2000
	s_cselect_b32 s4, s5, 0x88
	s_add_u32 s4, s0, s4
	s_addc_u32 s5, s1, 0
	s_ashr_i32 s14, s7, 31
	s_lshr_b32 s14, s14, 20
	s_add_i32 s14, s7, s14
	s_and_b32 s14, s14, 0xf000
	s_sub_i32 s7, s7, s14
	s_sext_i32_i16 s14, s7
	s_lshr_b32 s14, s14, 15
	s_bfe_u32 s16, s14, 0x4000c
	s_add_i32 s16, s7, s16
	s_and_b32 s16, s16, 0xfff0
	s_bfe_u32 s14, s14, 0x80008
	s_sub_i32 s16, s7, s16
	s_add_i32 s14, s7, s14
	s_sext_i32_i16 s18, s16
	s_sext_i32_i16 s16, s14
	s_and_b32 s14, s14, 0xff00
	s_load_dwordx2 s[4:5], s[4:5], 0x0
	s_ashr_i32 s16, s16, 8
	s_sub_i32 s7, s7, s14
	s_sext_i32_i16 s14, s7
	s_add_i32 s16, s16, 16
	s_bfe_u32 s14, s14, 0x4001b
	s_and_b32 s52, s16, 0xffff
	s_add_i32 s7, s7, s14
	s_lshl_b64 s[16:17], s[52:53], 24
	s_sext_i32_i16 s7, s7
	s_waitcnt lgkmcnt(0)
	s_add_u32 s14, s4, s16
	v_mov_b32_e32 v1, v0
	s_addc_u32 s16, s5, s17
	s_lshl_b32 s4, s7, 3
	v_ashrrev_i32_e32 v2, 3, v1
	s_and_b32 s4, s4, 0xffffff80
	v_and_b32_e32 v2, -4, v2
	s_waitcnt vmcnt(2)
	v_add_u32_e32 v4, s4, v2
	s_lshl_b32 s4, s18, 7
	s_ashr_i32 s5, s4, 31
	s_lshl_b64 s[4:5], s[4:5], 2
	s_add_u32 s4, s14, s4
	v_lshlrev_b32_e32 v1, 4, v1
	s_addc_u32 s5, s16, s5
	v_and_b32_e32 v2, 0x1f0, v1
	v_ashrrev_i32_e32 v5, 31, v4
	v_lshl_add_u64 v[6:7], s[4:5], 0, v[2:3]
	s_waitcnt vmcnt(1)
	v_lshlrev_b64 v[8:9], 13, v[4:5]
	v_lshl_add_u64 v[12:13], v[6:7], 0, v[8:9]
	v_or_b32_e32 v8, 1, v4
	v_ashrrev_i32_e32 v9, 31, v8
	v_lshlrev_b64 v[8:9], 13, v[8:9]
	v_lshl_add_u64 v[8:9], v[6:7], 0, v[8:9]
	global_load_dwordx4 v[20:23], v[12:13], off nt
	global_load_dwordx4 v[24:27], v[8:9], off nt
	v_or_b32_e32 v8, 2, v4
	v_or_b32_e32 v4, 3, v4
	v_ashrrev_i32_e32 v9, 31, v8
	v_ashrrev_i32_e32 v5, 31, v4
	v_lshlrev_b64 v[8:9], 13, v[8:9]
	v_lshlrev_b64 v[4:5], 13, v[4:5]
	v_lshl_add_u64 v[8:9], v[6:7], 0, v[8:9]
	v_lshl_add_u64 v[4:5], v[6:7], 0, v[4:5]
	global_load_dwordx4 v[28:31], v[8:9], off nt
	global_load_dwordx4 v[32:35], v[4:5], off nt
	v_add_co_u32_e32 v4, vcc, s94, v12
	s_mov_b32 s19, 0x82000
	s_nop 0
	v_addc_co_u32_e32 v5, vcc, 0, v13, vcc
	v_add_co_u32_e32 v8, vcc, s19, v12
	s_mov_b32 s4, 0x84000
	s_nop 0
	v_addc_co_u32_e32 v9, vcc, 0, v13, vcc
	v_add_co_u32_e32 v14, vcc, s4, v12
	s_mov_b32 s4, 0x86000
	s_nop 0
	v_addc_co_u32_e32 v15, vcc, 0, v13, vcc
	s_add_i32 s7, s6, 0x1cf0
	v_add_co_u32_e32 v16, vcc, s4, v12
	s_and_b32 s4, s7, 0xfffff000
	s_add_i32 s5, s6, 0x2cef
	s_cmpk_lt_u32 s5, 0x1fff
	s_cselect_b32 s5, s64, 0x80
	s_cmpk_lg_i32 s4, 0x2000
	s_cselect_b32 s4, s5, 0x88
	s_add_u32 s4, s0, s4
	s_addc_u32 s5, s1, 0
	s_ashr_i32 s14, s7, 31
	s_lshr_b32 s14, s14, 20
	s_add_i32 s14, s7, s14
	s_and_b32 s14, s14, 0xf000
	s_sub_i32 s7, s7, s14
	s_sext_i32_i16 s14, s7
	s_lshr_b32 s14, s14, 15
	s_bfe_u32 s16, s14, 0x4000c
	s_add_i32 s16, s7, s16
	s_and_b32 s16, s16, 0xfff0
	s_bfe_u32 s14, s14, 0x80008
	v_addc_co_u32_e32 v17, vcc, 0, v13, vcc
	s_sub_i32 s16, s7, s16
	s_add_i32 s14, s7, s14
	global_load_dwordx4 v[4:7], v[4:5], off nt
	s_nop 0
	global_load_dwordx4 v[8:11], v[8:9], off nt
	s_nop 0
	global_load_dwordx4 v[12:15], v[14:15], off nt
	s_nop 0
	global_load_dwordx4 v[16:19], v[16:17], off nt
	s_sext_i32_i16 s18, s16
	s_sext_i32_i16 s16, s14
	s_and_b32 s14, s14, 0xff00
	s_load_dwordx2 s[4:5], s[4:5], 0x0
	s_ashr_i32 s16, s16, 8
	s_sub_i32 s7, s7, s14
	s_sext_i32_i16 s14, s7
	s_add_i32 s16, s16, 16
	s_bfe_u32 s14, s14, 0x4001b
	s_and_b32 s52, s16, 0xffff
	s_add_i32 s7, s7, s14
	s_lshl_b64 s[16:17], s[52:53], 24
	s_sext_i32_i16 s7, s7
	s_waitcnt lgkmcnt(0)
	s_add_u32 s14, s4, s16
	v_mov_b32_e32 v1, v0
	s_addc_u32 s16, s5, s17
	s_lshl_b32 s4, s7, 3
	v_ashrrev_i32_e32 v2, 3, v1
	s_and_b32 s4, s4, 0xffffff80
	v_and_b32_e32 v2, -4, v2
	v_add_u32_e32 v44, s4, v2
	s_lshl_b32 s4, s18, 7
	s_ashr_i32 s5, s4, 31
	s_lshl_b64 s[4:5], s[4:5], 2
	s_add_u32 s4, s14, s4
	v_lshlrev_b32_e32 v1, 4, v1
	s_addc_u32 s5, s16, s5
	v_and_b32_e32 v2, 0x1f0, v1
	v_ashrrev_i32_e32 v45, 31, v44
	v_lshl_add_u64 v[46:47], s[4:5], 0, v[2:3]
	v_lshlrev_b64 v[36:37], 13, v[44:45]
	v_lshl_add_u64 v[48:49], v[46:47], 0, v[36:37]
	v_or_b32_e32 v36, 1, v44
	v_or_b32_e32 v50, 2, v44
	v_or_b32_e32 v44, 3, v44
	v_ashrrev_i32_e32 v37, 31, v36
	v_ashrrev_i32_e32 v51, 31, v50
	v_ashrrev_i32_e32 v45, 31, v44
	v_lshlrev_b64 v[36:37], 13, v[36:37]
	v_lshlrev_b64 v[50:51], 13, v[50:51]
	v_lshlrev_b64 v[44:45], 13, v[44:45]
	v_lshl_add_u64 v[40:41], v[46:47], 0, v[36:37]
	v_lshl_add_u64 v[50:51], v[46:47], 0, v[50:51]
	v_lshl_add_u64 v[44:45], v[46:47], 0, v[44:45]
	global_load_dwordx4 v[36:39], v[48:49], off nt
	s_nop 0
	global_load_dwordx4 v[40:43], v[40:41], off nt
	s_nop 0
	global_load_dwordx4 v[72:75], v[50:51], off nt
	global_load_dwordx4 v[76:79], v[44:45], off nt
	v_add_co_u32_e32 v44, vcc, s94, v48
	s_mov_b32 s4, 0
	s_nop 0
	v_addc_co_u32_e32 v45, vcc, 0, v49, vcc
	v_add_co_u32_e32 v46, vcc, s19, v48
	s_add_i32 s5, s6, 0x2d0f
	s_nop 0
	v_addc_co_u32_e32 v47, vcc, 0, v49, vcc
	global_load_dwordx4 v[84:87], v[44:45], off nt
	global_load_dwordx4 v[88:91], v[46:47], off nt
	v_add_co_u32_e32 v44, vcc, 0x84000, v48
	s_nop 1
	v_addc_co_u32_e32 v45, vcc, 0, v49, vcc
	v_add_co_u32_e32 v46, vcc, 0x86000, v48
	s_nop 1
	v_addc_co_u32_e32 v47, vcc, 0, v49, vcc
	global_load_dwordx4 v[92:95], v[44:45], off nt
	global_load_dwordx4 v[96:99], v[46:47], off nt
	s_waitcnt vmcnt(0)
	s_branch .LBB0_777

; DEVI int opaque_tid() { int t = threadIdx.x; asm volatile("" : "+v"(t)); return t; }
; DEVI void cvt8_load(const Params& p, int L, int t, CvtIn& in) {
;     const int which = t / 4096, r = t % 4096, le = L * 16 + r / 256, kt = (r % 256) / 16, nt = r % 16;
;     const float* src = (which == 2 ? p.w_down : (which == 0 ? p.w_gate : p.w_up)) + (size_t)le * 2048 * 2048;
;     const int tid = opaque_tid(), nq = tid & 31, kq0 = tid >> 5;
; #pragma unroll
;     for (int it = 0; it < 2; ++it)
; #pragma unroll
;         for (int kk = 0; kk < 4; ++kk) in.v[it * 4 + kk] = __builtin_nontemporal_load((const f32x4*)(src + (size_t)(kt * 128 + (kq0 + it * 16) * 4 + kk) * 2048 + nt * 128 + nq * 4));
; }
; DEVI void cvt8_stream3(const Params& p, int L, int t0, int step, int count, char* smem) {
;     ...
;     for (int i = 0; i < count; ++i) { CvtIn c;
;         if (i + 2 < count) cvt8_load(p, L, t0 + (i + 2) * step, c);
;         cvt8_finish(p, L, t0 + i * step, a, smem);
;         a = b; b = c; }
.LBB0_777:
	s_waitcnt vmcnt(2)
	v_mov_b64_e32 v[44:45], v[96:97]
	v_mov_b64_e32 v[48:49], v[92:93]
	v_mov_b64_e32 v[52:53], v[88:89]
	v_mov_b64_e32 v[56:57], v[84:85]
	v_mov_b64_e32 v[60:61], v[76:77]
	v_mov_b64_e32 v[64:65], v[72:73]
	v_mov_b64_e32 v[70:71], v[42:43]
	v_mov_b64_e32 v[82:83], v[38:39]
	v_mov_b64_e32 v[46:47], v[98:99]
	v_mov_b64_e32 v[50:51], v[94:95]
	v_mov_b64_e32 v[54:55], v[90:91]
	v_mov_b64_e32 v[58:59], v[86:87]
	v_mov_b64_e32 v[62:63], v[78:79]
	v_mov_b64_e32 v[66:67], v[74:75]
	v_mov_b64_e32 v[68:69], v[40:41]
	s_cmpk_gt_u32 s4, 0x4b
	v_mov_b64_e32 v[80:81], v[36:37]
	s_cbranch_scc1 .LBB0_779
	s_add_i32 s7, s5, 0xfffff001
	s_and_b32 s14, s7, 0xfffff000
	s_cmpk_lt_u32 s5, 0x1fff
	s_cselect_b32 s16, s64, 0x80
	s_cmpk_lg_i32 s14, 0x2000
	s_cselect_b32 s14, s16, 0x88
	s_add_u32 s16, s0, s14
	s_addc_u32 s17, s1, 0
	s_ashr_i32 s14, s7, 31
	s_lshr_b32 s14, s14, 20
	s_add_i32 s14, s7, s14
	s_and_b32 s14, s14, 0xf000
	s_sub_i32 s7, s7, s14
	s_sext_i32_i16 s14, s7
	s_lshr_b32 s14, s14, 15
	s_bfe_u32 s18, s14, 0x4000c
	s_add_i32 s18, s7, s18
	s_and_b32 s18, s18, 0xfff0
	s_bfe_u32 s14, s14, 0x80008
	s_sub_i32 s18, s7, s18
	s_add_i32 s14, s7, s14
	s_sext_i32_i16 s23, s18
	s_sext_i32_i16 s18, s14
	s_and_b32 s14, s14, 0xff00
	s_load_dwordx2 s[16:17], s[16:17], 0x0
	s_ashr_i32 s18, s18, 8
	s_sub_i32 s7, s7, s14
	s_sext_i32_i16 s14, s7
	s_add_i32 s18, s18, 16
	s_bfe_u32 s14, s14, 0x4001b
	s_and_b32 s52, s18, 0xffff
	s_add_i32 s7, s7, s14
	s_lshl_b64 s[18:19], s[52:53], 24
	s_waitcnt lgkmcnt(0)
	s_add_u32 s14, s16, s18
	s_sext_i32_i16 s7, s7
	s_addc_u32 s18, s17, s19
	v_mov_b32_e32 v1, v0
	s_lshl_b32 s16, s23, 7
	s_lshl_b32 s7, s7, 3
	v_ashrrev_i32_e32 v2, 3, v1
	s_ashr_i32 s17, s16, 31
	s_and_b32 s7, s7, 0xffffff80
	v_and_b32_e32 v2, -4, v2
	s_lshl_b64 s[16:17], s[16:17], 2
	v_add_u32_e32 v72, s7, v2
	s_add_u32 s16, s14, s16
	v_lshlrev_b32_e32 v1, 4, v1
	s_addc_u32 s17, s18, s17
	v_and_b32_e32 v2, 0x1f0, v1
	v_ashrrev_i32_e32 v73, 31, v72
	v_lshl_add_u64 v[74:75], s[16:17], 0, v[2:3]
	v_lshlrev_b64 v[36:37], 13, v[72:73]
	v_lshl_add_u64 v[92:93], v[74:75], 0, v[36:37]
	v_add_co_u32_e32 v84, vcc, s94, v92
	v_or_b32_e32 v36, 1, v72
	s_nop 0
	v_addc_co_u32_e32 v85, vcc, 0, v93, vcc
	v_add_co_u32_e32 v88, vcc, 0x82000, v92
	v_or_b32_e32 v76, 2, v72
	s_nop 0
	v_addc_co_u32_e32 v89, vcc, 0, v93, vcc
	v_or_b32_e32 v72, 3, v72
	v_add_co_u32_e32 v94, vcc, 0x84000, v92
	v_ashrrev_i32_e32 v37, 31, v36
	v_ashrrev_i32_e32 v77, 31, v76
	v_ashrrev_i32_e32 v73, 31, v72
	v_addc_co_u32_e32 v95, vcc, 0, v93, vcc
	v_lshlrev_b64 v[36:37], 13, v[36:37]
	v_lshlrev_b64 v[76:77], 13, v[76:77]
	v_lshlrev_b64 v[72:73], 13, v[72:73]
	v_add_co_u32_e32 v96, vcc, 0x86000, v92
	v_lshl_add_u64 v[40:41], v[74:75], 0, v[36:37]
	v_lshl_add_u64 v[76:77], v[74:75], 0, v[76:77]
	v_lshl_add_u64 v[78:79], v[74:75], 0, v[72:73]
	v_addc_co_u32_e32 v97, vcc, 0, v93, vcc
	global_load_dwordx4 v[36:39], v[92:93], off nt
	s_nop 0
	global_load_dwordx4 v[40:43], v[40:41], off nt
	s_nop 0
	global_load_dwordx4 v[72:75], v[76:77], off nt
	s_nop 0
	global_load_dwordx4 v[76:79], v[78:79], off nt
	s_nop 0
	global_load_dwordx4 v[84:87], v[84:85], off nt
	s_nop 0
	global_load_dwordx4 v[88:91], v[88:89], off nt
	s_nop 0
	global_load_dwordx4 v[92:95], v[94:95], off nt
	s_nop 0
	global_load_dwordx4 v[96:99], v[96:97], off nt

; DEVI int obid() { int b = blockIdx.x; asm volatile("" : "+s"(b)); return b; }
; DEVI void cvt8_stream3(const Params& p, int L, int t0, int step, int count, char* smem) {
;     if (count <= 0) return;
;     CvtIn a, b; cvt8_load(p, L, t0, a);
;     if (count > 1) cvt8_load(p, L, t0 + step, b);
; #pragma nounroll
;     for (int i = 0; i < count; ++i) { CvtIn c;
;         if (i + 2 < count) cvt8_load(p, L, t0 + (i + 2) * step, c);
;         cvt8_finish(p, L, t0 + i * step, a, smem);
;         a = b; b = c; }
; DEVI void phase_l4(const Params& p, int l, char* smem) {
;     ...
;     if (conv) { const int w = obid() - (256 - L4NC);
;         if (l == 0) { cvt8_stream3(p, 0, T0C + w, L4NC, L4C0_PER, smem); cvt8_stream3(p, 1, T1C + w, L4NC, L4C1_PER, smem); }
;         else cvt8_stream3(p, 1, T1D0 + w, L4NC, L4C2_PER, smem);
.LBB0_784:
	s_and_b64 vcc, exec, s[16:17]
	s_cbranch_vccz .LBB0_801
	s_add_i32 s7, s6, 0x1fd0
	s_and_b32 s4, s7, 0xfffff000
	s_add_i32 s5, s6, 0x2fcf
	s_cmpk_lt_u32 s5, 0x1fff
	s_cselect_b32 s5, s64, 0x80
	s_cmpk_lg_i32 s4, 0x2000
	s_cselect_b32 s4, s5, 0x88
	s_add_u32 s4, s0, s4
	s_addc_u32 s5, s1, 0
	s_ashr_i32 s14, s7, 31
	s_lshr_b32 s14, s14, 20
	s_add_i32 s14, s7, s14
	s_and_b32 s14, s14, 0xf000
	s_sub_i32 s7, s7, s14
	s_sext_i32_i16 s14, s7
	s_lshr_b32 s14, s14, 15
	s_bfe_u32 s16, s14, 0x4000c
	s_add_i32 s16, s7, s16
	s_and_b32 s16, s16, 0xfff0
	s_sub_i32 s16, s7, s16
	s_bfe_u32 s14, s14, 0x80008
	s_sext_i32_i16 s18, s16
	s_add_i32 s16, s7, s14
	s_sext_i32_i16 s14, s16
	s_and_b32 s16, s16, 0xff00
	s_sub_i32 s7, s7, s16
	s_load_dwordx2 s[4:5], s[4:5], 0x0
	s_sext_i32_i16 s16, s7
	s_lshr_b32 s14, s14, 8
	s_bfe_u32 s16, s16, 0x4001b
	s_add_i32 s7, s7, s16
	s_bfe_i64 s[16:17], s[14:15], 0x100000
	s_lshl_b64 s[16:17], s[16:17], 24
	s_sext_i32_i16 s7, s7
	s_waitcnt lgkmcnt(0)
	s_add_u32 s14, s4, s16
	v_mov_b32_e32 v1, v0
	s_addc_u32 s16, s5, s17
	s_lshl_b32 s4, s7, 3
	v_ashrrev_i32_e32 v2, 3, v1
	s_and_b32 s4, s4, 0xffffff80
	v_and_b32_e32 v2, -4, v2
	s_waitcnt vmcnt(2)
	v_add_u32_e32 v4, s4, v2
	s_lshl_b32 s4, s18, 7
	s_ashr_i32 s5, s4, 31
	s_lshl_b64 s[4:5], s[4:5], 2
	s_add_u32 s4, s14, s4
	v_lshlrev_b32_e32 v1, 4, v1
	s_addc_u32 s5, s16, s5
	v_and_b32_e32 v2, 0x1f0, v1
	v_ashrrev_i32_e32 v5, 31, v4
	v_lshl_add_u64 v[6:7], s[4:5], 0, v[2:3]
	s_waitcnt vmcnt(1)
	v_lshlrev_b64 v[8:9], 13, v[4:5]
	v_lshl_add_u64 v[12:13], v[6:7], 0, v[8:9]
	v_or_b32_e32 v8, 1, v4
	v_ashrrev_i32_e32 v9, 31, v8
	v_lshlrev_b64 v[8:9], 13, v[8:9]
	v_lshl_add_u64 v[8:9], v[6:7], 0, v[8:9]
	global_load_dwordx4 v[20:23], v[12:13], off nt
	global_load_dwordx4 v[24:27], v[8:9], off nt
	v_or_b32_e32 v8, 2, v4
	v_or_b32_e32 v4, 3, v4
	v_ashrrev_i32_e32 v9, 31, v8
	v_ashrrev_i32_e32 v5, 31, v4
	v_lshlrev_b64 v[8:9], 13, v[8:9]
	v_lshlrev_b64 v[4:5], 13, v[4:5]
	v_lshl_add_u64 v[8:9], v[6:7], 0, v[8:9]
	v_lshl_add_u64 v[4:5], v[6:7], 0, v[4:5]
	global_load_dwordx4 v[28:31], v[8:9], off nt
	global_load_dwordx4 v[32:35], v[4:5], off nt
	v_add_co_u32_e32 v4, vcc, s94, v12
	s_mov_b32 s19, 0x82000
	s_nop 0
	v_addc_co_u32_e32 v5, vcc, 0, v13, vcc
	v_add_co_u32_e32 v8, vcc, s19, v12
	s_mov_b32 s4, 0x84000
	s_nop 0
	v_addc_co_u32_e32 v9, vcc, 0, v13, vcc
	v_add_co_u32_e32 v14, vcc, s4, v12
	s_mov_b32 s4, 0x86000
	s_nop 0
	v_addc_co_u32_e32 v15, vcc, 0, v13, vcc
	s_add_i32 s7, s6, 0x1ff0
	v_add_co_u32_e32 v16, vcc, s4, v12
	s_and_b32 s4, s7, 0xfffff000
	s_add_i32 s5, s6, 0x2fef
	s_cmpk_lt_u32 s5, 0x1fff
	s_cselect_b32 s5, s64, 0x80
	s_cmpk_lg_i32 s4, 0x2000
	s_cselect_b32 s4, s5, 0x88
	s_add_u32 s4, s0, s4
	s_addc_u32 s5, s1, 0
	s_ashr_i32 s14, s7, 31
	s_lshr_b32 s14, s14, 20
	s_add_i32 s14, s7, s14
	s_and_b32 s14, s14, 0xf000
	s_sub_i32 s7, s7, s14
	s_sext_i32_i16 s14, s7
	s_lshr_b32 s14, s14, 15
	s_bfe_u32 s16, s14, 0x4000c
	s_add_i32 s16, s7, s16
	s_and_b32 s16, s16, 0xfff0
	s_sub_i32 s16, s7, s16
	s_bfe_u32 s14, s14, 0x80008
	s_sext_i32_i16 s18, s16
	s_add_i32 s16, s7, s14
	v_addc_co_u32_e32 v17, vcc, 0, v13, vcc
	s_sext_i32_i16 s14, s16
	s_and_b32 s16, s16, 0xff00
	global_load_dwordx4 v[4:7], v[4:5], off nt
	s_nop 0
	global_load_dwordx4 v[8:11], v[8:9], off nt
	s_nop 0
	global_load_dwordx4 v[12:15], v[14:15], off nt
	s_nop 0
	global_load_dwordx4 v[16:19], v[16:17], off nt
	s_sub_i32 s7, s7, s16
	s_load_dwordx2 s[4:5], s[4:5], 0x0
	s_sext_i32_i16 s16, s7
	s_lshr_b32 s14, s14, 8
	s_bfe_u32 s16, s16, 0x4001b
	s_add_i32 s7, s7, s16
	s_bfe_i64 s[16:17], s[14:15], 0x100000
	s_lshl_b64 s[16:17], s[16:17], 24
	s_sext_i32_i16 s7, s7
	s_waitcnt lgkmcnt(0)
	s_add_u32 s14, s4, s16
	v_mov_b32_e32 v1, v0
	s_addc_u32 s16, s5, s17
	s_lshl_b32 s4, s7, 3
	v_ashrrev_i32_e32 v2, 3, v1
	s_and_b32 s4, s4, 0xffffff80
	v_and_b32_e32 v2, -4, v2
	v_add_u32_e32 v44, s4, v2
	s_lshl_b32 s4, s18, 7
	s_ashr_i32 s5, s4, 31
	s_lshl_b64 s[4:5], s[4:5], 2
	s_add_u32 s4, s14, s4
	v_lshlrev_b32_e32 v1, 4, v1
	s_addc_u32 s5, s16, s5
	v_and_b32_e32 v2, 0x1f0, v1
	v_ashrrev_i32_e32 v45, 31, v44
	v_lshl_add_u64 v[46:47], s[4:5], 0, v[2:3]
	v_lshlrev_b64 v[36:37], 13, v[44:45]
	v_lshl_add_u64 v[48:49], v[46:47], 0, v[36:37]
	v_or_b32_e32 v36, 1, v44
	v_or_b32_e32 v50, 2, v44
	v_or_b32_e32 v44, 3, v44
	v_ashrrev_i32_e32 v37, 31, v36
	v_ashrrev_i32_e32 v51, 31, v50
	v_ashrrev_i32_e32 v45, 31, v44
	v_lshlrev_b64 v[36:37], 13, v[36:37]
	v_lshlrev_b64 v[50:51], 13, v[50:51]
	v_lshlrev_b64 v[44:45], 13, v[44:45]
	v_lshl_add_u64 v[40:41], v[46:47], 0, v[36:37]
	v_lshl_add_u64 v[50:51], v[46:47], 0, v[50:51]
	v_lshl_add_u64 v[44:45], v[46:47], 0, v[44:45]
	global_load_dwordx4 v[36:39], v[48:49], off nt
	s_nop 0
	global_load_dwordx4 v[40:43], v[40:41], off nt
	s_nop 0
	global_load_dwordx4 v[72:75], v[50:51], off nt
	global_load_dwordx4 v[76:79], v[44:45], off nt
	v_add_co_u32_e32 v44, vcc, s94, v48
	s_mov_b32 s4, 0
	s_nop 0
	v_addc_co_u32_e32 v45, vcc, 0, v49, vcc
	v_add_co_u32_e32 v46, vcc, s19, v48
	s_add_i32 s5, s6, 0x300f
	s_nop 0
	v_addc_co_u32_e32 v47, vcc, 0, v49, vcc
	global_load_dwordx4 v[84:87], v[44:45], off nt
	global_load_dwordx4 v[88:91], v[46:47], off nt
	v_add_co_u32_e32 v44, vcc, 0x84000, v48
	s_nop 1
	v_addc_co_u32_e32 v45, vcc, 0, v49, vcc
	v_add_co_u32_e32 v46, vcc, 0x86000, v48
	s_nop 1
	v_addc_co_u32_e32 v47, vcc, 0, v49, vcc
	global_load_dwordx4 v[92:95], v[44:45], off nt
	global_load_dwordx4 v[96:99], v[46:47], off nt
	s_waitcnt vmcnt(0)
	s_branch .LBB0_787

; DEVI int opaque_tid() { int t = threadIdx.x; asm volatile("" : "+v"(t)); return t; }
; DEVI void cvt8_load(const Params& p, int L, int t, CvtIn& in) {
;     const int which = t / 4096, r = t % 4096, le = L * 16 + r / 256, kt = (r % 256) / 16, nt = r % 16;
;     const float* src = (which == 2 ? p.w_down : (which == 0 ? p.w_gate : p.w_up)) + (size_t)le * 2048 * 2048;
;     const int tid = opaque_tid(), nq = tid & 31, kq0 = tid >> 5;
; #pragma unroll
;     for (int it = 0; it < 2; ++it)
; #pragma unroll
;         for (int kk = 0; kk < 4; ++kk) in.v[it * 4 + kk] = __builtin_nontemporal_load((const f32x4*)(src + (size_t)(kt * 128 + (kq0 + it * 16) * 4 + kk) * 2048 + nt * 128 + nq * 4));
; }
; DEVI void cvt8_stream3(const Params& p, int L, int t0, int step, int count, char* smem) {
;     if (count <= 0) return;
;     CvtIn a, b; cvt8_load(p, L, t0, a);
;     if (count > 1) cvt8_load(p, L, t0 + step, b);
; #pragma nounroll
;     for (int i = 0; i < count; ++i) { CvtIn c;
;         if (i + 2 < count) cvt8_load(p, L, t0 + (i + 2) * step, c);
;         cvt8_finish(p, L, t0 + i * step, a, smem);
;         a = b; b = c; }
; }
.LBB0_787:
	s_waitcnt vmcnt(2)
	v_mov_b64_e32 v[44:45], v[96:97]
	v_mov_b64_e32 v[48:49], v[92:93]
	v_mov_b64_e32 v[52:53], v[88:89]
	v_mov_b64_e32 v[56:57], v[84:85]
	v_mov_b64_e32 v[60:61], v[76:77]
	v_mov_b64_e32 v[64:65], v[72:73]
	v_mov_b64_e32 v[70:71], v[42:43]
	v_mov_b64_e32 v[82:83], v[38:39]
	v_mov_b64_e32 v[46:47], v[98:99]
	v_mov_b64_e32 v[50:51], v[94:95]
	v_mov_b64_e32 v[54:55], v[90:91]
	v_mov_b64_e32 v[58:59], v[86:87]
	v_mov_b64_e32 v[62:63], v[78:79]
	v_mov_b64_e32 v[66:67], v[74:75]
	v_mov_b64_e32 v[68:69], v[40:41]
	s_cmp_gt_u32 s4, 47
	v_mov_b64_e32 v[80:81], v[36:37]
	s_cbranch_scc1 .LBB0_789
	s_add_i32 s7, s5, 0xfffff001
	s_and_b32 s14, s7, 0xfffff000
	s_cmpk_lt_u32 s5, 0x1fff
	s_cselect_b32 s16, s64, 0x80
	s_cmpk_lg_i32 s14, 0x2000
	s_cselect_b32 s14, s16, 0x88
	s_add_u32 s16, s0, s14
	s_addc_u32 s17, s1, 0
	s_ashr_i32 s14, s7, 31
	s_lshr_b32 s14, s14, 20
	s_add_i32 s14, s7, s14
	s_and_b32 s14, s14, 0xf000
	s_sub_i32 s7, s7, s14
	s_sext_i32_i16 s14, s7
	s_lshr_b32 s14, s14, 15
	s_bfe_u32 s18, s14, 0x4000c
	s_add_i32 s18, s7, s18
	s_and_b32 s18, s18, 0xfff0
	s_sub_i32 s18, s7, s18
	s_bfe_u32 s14, s14, 0x80008
	s_sext_i32_i16 s23, s18
	s_add_i32 s18, s7, s14
	s_sext_i32_i16 s14, s18
	s_and_b32 s18, s18, 0xff00
	s_sub_i32 s7, s7, s18
	s_load_dwordx2 s[16:17], s[16:17], 0x0
	s_sext_i32_i16 s18, s7
	s_lshr_b32 s14, s14, 8
	s_bfe_u32 s18, s18, 0x4001b
	s_add_i32 s7, s7, s18
	s_bfe_i64 s[18:19], s[14:15], 0x100000
	s_lshl_b64 s[18:19], s[18:19], 24
	s_waitcnt lgkmcnt(0)
	s_add_u32 s14, s16, s18
	s_sext_i32_i16 s7, s7
	s_addc_u32 s18, s17, s19
	v_mov_b32_e32 v1, v0
	s_lshl_b32 s16, s23, 7
	s_lshl_b32 s7, s7, 3
	v_ashrrev_i32_e32 v2, 3, v1
	s_ashr_i32 s17, s16, 31
	s_and_b32 s7, s7, 0xffffff80
	v_and_b32_e32 v2, -4, v2
	s_lshl_b64 s[16:17], s[16:17], 2
	v_add_u32_e32 v72, s7, v2
	s_add_u32 s16, s14, s16
	v_lshlrev_b32_e32 v1, 4, v1
	s_addc_u32 s17, s18, s17
	v_and_b32_e32 v2, 0x1f0, v1
	v_ashrrev_i32_e32 v73, 31, v72
	v_lshl_add_u64 v[74:75], s[16:17], 0, v[2:3]
	v_lshlrev_b64 v[36:37], 13, v[72:73]
	v_lshl_add_u64 v[92:93], v[74:75], 0, v[36:37]
	v_add_co_u32_e32 v84, vcc, s94, v92
	v_or_b32_e32 v36, 1, v72
	s_nop 0
	v_addc_co_u32_e32 v85, vcc, 0, v93, vcc
	v_add_co_u32_e32 v88, vcc, 0x82000, v92
	v_or_b32_e32 v76, 2, v72
	s_nop 0
	v_addc_co_u32_e32 v89, vcc, 0, v93, vcc
	v_or_b32_e32 v72, 3, v72
	v_add_co_u32_e32 v94, vcc, 0x84000, v92
	v_ashrrev_i32_e32 v37, 31, v36
	v_ashrrev_i32_e32 v77, 31, v76
	v_ashrrev_i32_e32 v73, 31, v72
	v_addc_co_u32_e32 v95, vcc, 0, v93, vcc
	v_lshlrev_b64 v[36:37], 13, v[36:37]
	v_lshlrev_b64 v[76:77], 13, v[76:77]
	v_lshlrev_b64 v[72:73], 13, v[72:73]
	v_add_co_u32_e32 v96, vcc, 0x86000, v92
	v_lshl_add_u64 v[40:41], v[74:75], 0, v[36:37]
	v_lshl_add_u64 v[76:77], v[74:75], 0, v[76:77]
	v_lshl_add_u64 v[78:79], v[74:75], 0, v[72:73]
	v_addc_co_u32_e32 v97, vcc, 0, v93, vcc
	global_load_dwordx4 v[36:39], v[92:93], off nt
	s_nop 0
	global_load_dwordx4 v[40:43], v[40:41], off nt
	s_nop 0
	global_load_dwordx4 v[72:75], v[76:77], off nt
	s_nop 0
	global_load_dwordx4 v[76:79], v[78:79], off nt
	s_nop 0
	global_load_dwordx4 v[84:87], v[84:85], off nt
	s_nop 0
	global_load_dwordx4 v[88:91], v[88:89], off nt
	s_nop 0
	global_load_dwordx4 v[92:95], v[94:95], off nt
	s_nop 0
	global_load_dwordx4 v[96:99], v[96:97], off nt

; DEVI int opaque_tid() { int t = threadIdx.x; asm volatile("" : "+v"(t)); return t; }
; DEVI void cvt8_load(const Params& p, int L, int t, CvtIn& in) {
;     const int which = t / 4096, r = t % 4096, le = L * 16 + r / 256, kt = (r % 256) / 16, nt = r % 16;
;     const float* src = (which == 2 ? p.w_down : (which == 0 ? p.w_gate : p.w_up)) + (size_t)le * 2048 * 2048;
;     const int tid = opaque_tid(), nq = tid & 31, kq0 = tid >> 5;
; #pragma unroll
;     for (int it = 0; it < 2; ++it)
; #pragma unroll
;         for (int kk = 0; kk < 4; ++kk) in.v[it * 4 + kk] = __builtin_nontemporal_load((const f32x4*)(src + (size_t)(kt * 128 + (kq0 + it * 16) * 4 + kk) * 2048 + nt * 128 + nq * 4));
; }
; DEVI void cvt8_stream3(const Params& p, int L, int t0, int step, int count, char* smem) {
;     if (count <= 0) return;
;     CvtIn a, b; cvt8_load(p, L, t0, a);
;     if (count > 1) cvt8_load(p, L, t0 + step, b);
.LBB0_793:
	s_add_i32 s7, s6, 0x1890
	s_and_b32 s4, s7, 0xfffff000
	s_add_i32 s5, s6, 0x288f
	s_cmpk_lt_u32 s5, 0x1fff
	s_cselect_b32 s5, s64, 0x80
	s_cmpk_lg_i32 s4, 0x2000
	s_cselect_b32 s4, s5, 0x88
	s_add_u32 s4, s0, s4
	s_addc_u32 s5, s1, 0
	s_ashr_i32 s14, s7, 31
	s_lshr_b32 s14, s14, 20
	s_add_i32 s14, s7, s14
	s_and_b32 s14, s14, 0xf000
	s_sub_i32 s7, s7, s14
	s_sext_i32_i16 s14, s7
	s_lshr_b32 s14, s14, 15
	s_bfe_u32 s16, s14, 0x4000c
	s_add_i32 s16, s7, s16
	s_and_b32 s16, s16, 0xfff0
	s_bfe_u32 s14, s14, 0x80008
	s_sub_i32 s16, s7, s16
	s_add_i32 s14, s7, s14
	s_sext_i32_i16 s18, s16
	s_sext_i32_i16 s16, s14
	s_and_b32 s14, s14, 0xff00
	s_load_dwordx2 s[4:5], s[4:5], 0x0
	s_ashr_i32 s16, s16, 8
	s_sub_i32 s7, s7, s14
	s_sext_i32_i16 s14, s7
	s_add_i32 s16, s16, 16
	s_bfe_u32 s14, s14, 0x4001b
	s_and_b32 s52, s16, 0xffff
	s_add_i32 s7, s7, s14
	s_lshl_b64 s[16:17], s[52:53], 24
	s_sext_i32_i16 s7, s7
	s_waitcnt lgkmcnt(0)
	s_add_u32 s14, s4, s16
	v_mov_b32_e32 v1, v0
	s_addc_u32 s16, s5, s17
	s_lshl_b32 s4, s7, 3
	v_ashrrev_i32_e32 v2, 3, v1
	s_and_b32 s4, s4, 0xffffff80
	v_and_b32_e32 v2, -4, v2
	v_add_u32_e32 v4, s4, v2
	s_lshl_b32 s4, s18, 7
	s_ashr_i32 s5, s4, 31
	s_lshl_b64 s[4:5], s[4:5], 2
	s_add_u32 s4, s14, s4
	v_lshlrev_b32_e32 v1, 4, v1
	s_addc_u32 s5, s16, s5
	v_and_b32_e32 v2, 0x1f0, v1
	v_ashrrev_i32_e32 v5, 31, v4
	v_lshl_add_u64 v[6:7], s[4:5], 0, v[2:3]
	v_lshlrev_b64 v[8:9], 13, v[4:5]
	v_lshl_add_u64 v[12:13], v[6:7], 0, v[8:9]
	v_or_b32_e32 v8, 1, v4
	v_ashrrev_i32_e32 v9, 31, v8
	v_lshlrev_b64 v[8:9], 13, v[8:9]
	v_lshl_add_u64 v[8:9], v[6:7], 0, v[8:9]
	global_load_dwordx4 v[20:23], v[12:13], off nt
	global_load_dwordx4 v[24:27], v[8:9], off nt
	v_or_b32_e32 v8, 2, v4
	v_or_b32_e32 v4, 3, v4
	v_ashrrev_i32_e32 v9, 31, v8
	v_ashrrev_i32_e32 v5, 31, v4
	v_lshlrev_b64 v[8:9], 13, v[8:9]
	v_lshlrev_b64 v[4:5], 13, v[4:5]
	v_lshl_add_u64 v[8:9], v[6:7], 0, v[8:9]
	v_lshl_add_u64 v[4:5], v[6:7], 0, v[4:5]
	global_load_dwordx4 v[28:31], v[8:9], off nt
	global_load_dwordx4 v[32:35], v[4:5], off nt
	v_add_co_u32_e32 v4, vcc, s94, v12
	s_mov_b32 s4, 0x82000
	s_nop 0
	v_addc_co_u32_e32 v5, vcc, 0, v13, vcc
	v_add_co_u32_e32 v8, vcc, s4, v12
	s_mov_b32 s4, 0x84000
	s_nop 0
	v_addc_co_u32_e32 v9, vcc, 0, v13, vcc
	v_add_co_u32_e32 v14, vcc, s4, v12
	s_mov_b32 s4, 0x86000
	s_nop 0
	v_addc_co_u32_e32 v15, vcc, 0, v13, vcc
	s_add_i32 s7, s6, 0x18b0
	v_add_co_u32_e32 v16, vcc, s4, v12
	s_and_b32 s4, s7, 0xfffff000
	s_add_i32 s5, s6, 0x28af
	s_cmpk_lt_u32 s5, 0x1fff
	s_cselect_b32 s5, s64, 0x80
	s_cmpk_lg_i32 s4, 0x2000
	s_cselect_b32 s4, s5, 0x88
	s_add_u32 s4, s0, s4
	s_addc_u32 s5, s1, 0
	s_ashr_i32 s14, s7, 31
	s_lshr_b32 s14, s14, 20
	s_add_i32 s14, s7, s14
	s_and_b32 s14, s14, 0xf000
	s_sub_i32 s7, s7, s14
	s_sext_i32_i16 s14, s7
	s_lshr_b32 s14, s14, 15
	s_bfe_u32 s16, s14, 0x4000c
	s_add_i32 s16, s7, s16
	s_and_b32 s16, s16, 0xfff0
	s_bfe_u32 s14, s14, 0x80008
	v_addc_co_u32_e32 v17, vcc, 0, v13, vcc
	s_sub_i32 s16, s7, s16
	s_add_i32 s14, s7, s14
	global_load_dwordx4 v[4:7], v[4:5], off nt
	s_nop 0
	global_load_dwordx4 v[8:11], v[8:9], off nt
	s_nop 0
	global_load_dwordx4 v[12:15], v[14:15], off nt
	s_nop 0
	global_load_dwordx4 v[16:19], v[16:17], off nt
	s_sext_i32_i16 s18, s16
	s_sext_i32_i16 s16, s14
	s_and_b32 s14, s14, 0xff00
	s_load_dwordx2 s[4:5], s[4:5], 0x0
	s_ashr_i32 s16, s16, 8
	s_sub_i32 s7, s7, s14
	s_sext_i32_i16 s14, s7
	s_add_i32 s16, s16, 16
	s_bfe_u32 s14, s14, 0x4001b
	s_and_b32 s52, s16, 0xffff
	s_add_i32 s7, s7, s14
	s_lshl_b64 s[16:17], s[52:53], 24
	s_sext_i32_i16 s7, s7
	s_waitcnt lgkmcnt(0)
	s_add_u32 s14, s4, s16
	v_mov_b32_e32 v1, v0
	s_addc_u32 s16, s5, s17
	s_lshl_b32 s4, s7, 3
	v_ashrrev_i32_e32 v2, 3, v1
	s_and_b32 s4, s4, 0xffffff80
	v_and_b32_e32 v2, -4, v2
	v_add_u32_e32 v44, s4, v2
	s_lshl_b32 s4, s18, 7
	s_ashr_i32 s5, s4, 31
	s_lshl_b64 s[4:5], s[4:5], 2
	s_add_u32 s4, s14, s4
	v_lshlrev_b32_e32 v1, 4, v1
	s_addc_u32 s5, s16, s5
	v_and_b32_e32 v2, 0x1f0, v1
	v_ashrrev_i32_e32 v45, 31, v44
	v_lshl_add_u64 v[46:47], s[4:5], 0, v[2:3]
	s_waitcnt vmcnt(17)
	v_lshlrev_b64 v[36:37], 13, v[44:45]
	v_lshl_add_u64 v[48:49], v[46:47], 0, v[36:37]
	v_or_b32_e32 v36, 1, v44
	v_or_b32_e32 v50, 2, v44
	v_or_b32_e32 v44, 3, v44
	v_ashrrev_i32_e32 v37, 31, v36
	v_ashrrev_i32_e32 v51, 31, v50
	v_ashrrev_i32_e32 v45, 31, v44
	v_lshlrev_b64 v[36:37], 13, v[36:37]
	v_lshlrev_b64 v[50:51], 13, v[50:51]
	v_lshlrev_b64 v[44:45], 13, v[44:45]
	s_waitcnt vmcnt(16)
	v_lshl_add_u64 v[40:41], v[46:47], 0, v[36:37]
	v_lshl_add_u64 v[50:51], v[46:47], 0, v[50:51]
	v_lshl_add_u64 v[44:45], v[46:47], 0, v[44:45]
	global_load_dwordx4 v[36:39], v[48:49], off nt
	s_nop 0
	global_load_dwordx4 v[40:43], v[40:41], off nt
	s_nop 0
	global_load_dwordx4 v[72:75], v[50:51], off nt
	global_load_dwordx4 v[76:79], v[44:45], off nt
	v_add_co_u32_e32 v44, vcc, s94, v48
	s_mov_b32 s4, 0
	s_nop 0
	v_addc_co_u32_e32 v45, vcc, 0, v49, vcc
	v_add_co_u32_e32 v46, vcc, 0x82000, v48
	s_add_i32 s5, s6, 0x28cf
	s_nop 0
	v_addc_co_u32_e32 v47, vcc, 0, v49, vcc
	global_load_dwordx4 v[84:87], v[44:45], off nt
	global_load_dwordx4 v[88:91], v[46:47], off nt
	v_add_co_u32_e32 v44, vcc, 0x84000, v48
	s_nop 1
	v_addc_co_u32_e32 v45, vcc, 0, v49, vcc
	v_add_co_u32_e32 v46, vcc, 0x86000, v48
	s_nop 1
	v_addc_co_u32_e32 v47, vcc, 0, v49, vcc
	global_load_dwordx4 v[92:95], v[44:45], off nt
	global_load_dwordx4 v[96:99], v[46:47], off nt
	s_waitcnt vmcnt(0)
	s_branch .LBB0_795

; DEVI int opaque_tid() { int t = threadIdx.x; asm volatile("" : "+v"(t)); return t; }
; DEVI void cvt8_load(const Params& p, int L, int t, CvtIn& in) {
;     const int which = t / 4096, r = t % 4096, le = L * 16 + r / 256, kt = (r % 256) / 16, nt = r % 16;
;     const float* src = (which == 2 ? p.w_down : (which == 0 ? p.w_gate : p.w_up)) + (size_t)le * 2048 * 2048;
;     const int tid = opaque_tid(), nq = tid & 31, kq0 = tid >> 5;
; #pragma unroll
;     for (int it = 0; it < 2; ++it)
; #pragma unroll
;         for (int kk = 0; kk < 4; ++kk) in.v[it * 4 + kk] = __builtin_nontemporal_load((const f32x4*)(src + (size_t)(kt * 128 + (kq0 + it * 16) * 4 + kk) * 2048 + nt * 128 + nq * 4));
; }
; DEVI void cvt8_stream3(const Params& p, int L, int t0, int step, int count, char* smem) {
;     if (count <= 0) return;
;     CvtIn a, b; cvt8_load(p, L, t0, a);
;     if (count > 1) cvt8_load(p, L, t0 + step, b);
; #pragma nounroll
;     for (int i = 0; i < count; ++i) { CvtIn c;
;         if (i + 2 < count) cvt8_load(p, L, t0 + (i + 2) * step, c);
;         cvt8_finish(p, L, t0 + i * step, a, smem);
;         a = b; b = c; }
; }
.LBB0_795:
	s_waitcnt vmcnt(2)
	v_mov_b64_e32 v[44:45], v[96:97]
	v_mov_b64_e32 v[48:49], v[92:93]
	v_mov_b64_e32 v[52:53], v[88:89]
	v_mov_b64_e32 v[56:57], v[84:85]
	v_mov_b64_e32 v[60:61], v[76:77]
	v_mov_b64_e32 v[64:65], v[72:73]
	v_mov_b64_e32 v[70:71], v[42:43]
	v_mov_b64_e32 v[82:83], v[38:39]
	v_mov_b64_e32 v[46:47], v[98:99]
	v_mov_b64_e32 v[50:51], v[94:95]
	v_mov_b64_e32 v[54:55], v[90:91]
	v_mov_b64_e32 v[58:59], v[86:87]
	v_mov_b64_e32 v[62:63], v[78:79]
	v_mov_b64_e32 v[66:67], v[74:75]
	v_mov_b64_e32 v[68:69], v[40:41]
	s_cmp_gt_u32 s4, 31
	v_mov_b64_e32 v[80:81], v[36:37]
	s_cbranch_scc1 .LBB0_797
	s_add_i32 s14, s5, 0xfffff001
	s_and_b32 s6, s14, 0xfffff000
	s_cmpk_lt_u32 s5, 0x1fff
	s_cselect_b32 s7, s64, 0x80
	s_cmpk_lg_i32 s6, 0x2000
	s_cselect_b32 s6, s7, 0x88
	s_add_u32 s6, s0, s6
	s_addc_u32 s7, s1, 0
	s_ashr_i32 s16, s14, 31
	s_lshr_b32 s16, s16, 20
	s_add_i32 s16, s14, s16
	s_and_b32 s16, s16, 0xf000
	s_sub_i32 s14, s14, s16
	s_sext_i32_i16 s16, s14
	s_lshr_b32 s16, s16, 15
	s_bfe_u32 s17, s16, 0x4000c
	s_add_i32 s17, s14, s17
	s_and_b32 s17, s17, 0xfff0
	s_bfe_u32 s16, s16, 0x80008
	s_sub_i32 s17, s14, s17
	s_add_i32 s16, s14, s16
	s_sext_i32_i16 s18, s17
	s_sext_i32_i16 s17, s16
	s_and_b32 s16, s16, 0xff00
	s_load_dwordx2 s[6:7], s[6:7], 0x0
	s_ashr_i32 s17, s17, 8
	s_sub_i32 s14, s14, s16
	s_sext_i32_i16 s16, s14
	s_add_i32 s17, s17, 16
	s_bfe_u32 s16, s16, 0x4001b
	s_and_b32 s52, s17, 0xffff
	s_add_i32 s14, s14, s16
	s_lshl_b64 s[16:17], s[52:53], 24
	s_sext_i32_i16 s14, s14
	s_waitcnt lgkmcnt(0)
	s_add_u32 s16, s6, s16
	v_mov_b32_e32 v1, v0
	s_addc_u32 s17, s7, s17
	s_lshl_b32 s6, s14, 3
	v_ashrrev_i32_e32 v2, 3, v1
	s_and_b32 s6, s6, 0xffffff80
	v_and_b32_e32 v2, -4, v2
	v_add_u32_e32 v72, s6, v2
	s_lshl_b32 s6, s18, 7
	s_ashr_i32 s7, s6, 31
	s_lshl_b64 s[6:7], s[6:7], 2
	s_add_u32 s6, s16, s6
	v_lshlrev_b32_e32 v1, 4, v1
	s_addc_u32 s7, s17, s7
	v_and_b32_e32 v2, 0x1f0, v1
	v_ashrrev_i32_e32 v73, 31, v72
	v_lshl_add_u64 v[74:75], s[6:7], 0, v[2:3]
	v_lshlrev_b64 v[36:37], 13, v[72:73]
	v_lshl_add_u64 v[92:93], v[74:75], 0, v[36:37]
	v_add_co_u32_e32 v84, vcc, s94, v92
	v_or_b32_e32 v36, 1, v72
	s_nop 0
	v_addc_co_u32_e32 v85, vcc, 0, v93, vcc
	v_add_co_u32_e32 v88, vcc, 0x82000, v92
	v_or_b32_e32 v76, 2, v72
	s_nop 0
	v_addc_co_u32_e32 v89, vcc, 0, v93, vcc
	v_or_b32_e32 v72, 3, v72
	v_add_co_u32_e32 v94, vcc, 0x84000, v92
	v_ashrrev_i32_e32 v37, 31, v36
	v_ashrrev_i32_e32 v77, 31, v76
	v_ashrrev_i32_e32 v73, 31, v72
	v_addc_co_u32_e32 v95, vcc, 0, v93, vcc
	v_lshlrev_b64 v[36:37], 13, v[36:37]
	v_lshlrev_b64 v[76:77], 13, v[76:77]
	v_lshlrev_b64 v[72:73], 13, v[72:73]
	v_add_co_u32_e32 v96, vcc, 0x86000, v92
	v_lshl_add_u64 v[40:41], v[74:75], 0, v[36:37]
	v_lshl_add_u64 v[76:77], v[74:75], 0, v[76:77]
	v_lshl_add_u64 v[78:79], v[74:75], 0, v[72:73]
	v_addc_co_u32_e32 v97, vcc, 0, v93, vcc
	global_load_dwordx4 v[36:39], v[92:93], off nt
	s_nop 0
	global_load_dwordx4 v[40:43], v[40:41], off nt
	s_nop 0
	global_load_dwordx4 v[72:75], v[76:77], off nt
	s_nop 0
	global_load_dwordx4 v[76:79], v[78:79], off nt
	s_nop 0
	global_load_dwordx4 v[84:87], v[84:85], off nt
	s_nop 0
	global_load_dwordx4 v[88:91], v[88:89], off nt
	s_nop 0
	global_load_dwordx4 v[92:95], v[94:95], off nt
	s_nop 0
	global_load_dwordx4 v[96:99], v[96:97], off nt
